# indexer scoring blocks rewritten with two MFMA accumulators so head h+1 MFMAs issue under head h ReLU/weighting VALU
# speedup vs baseline: 1.0017x; 1.0017x over previous
; __device__ __forceinline__ float relu_i(float p) { const int i = __float_as_int(p); return __int_as_float(i > 0 ? i : 0); }
; __device__ __forceinline__ void idx_scores_k(f32x16& sc, const bf16x8 (&kf)[4], const bf16x8 (&qf)[16], const f32x4& w) {
;     f32x16 p0 = f32x16{}, p1 = f32x16{};
; #pragma unroll
;     for (int d0 = 0; d0 < 4; ++d0) p0 = __builtin_amdgcn_mfma_f32_32x32x16_bf16(kf[d0], qf[d0], p0, 0, 0, 0);
; #pragma unroll
;     for (int d0 = 0; d0 < 4; ++d0) p1 = __builtin_amdgcn_mfma_f32_32x32x16_bf16(kf[d0], qf[4 + d0], p1, 0, 0, 0);
; #pragma unroll
;     for (int r = 0; r < 16; ++r) sc[r] = w[0] * relu_i(p0[r]);
;     p0 = f32x16{};
; #pragma unroll
;     for (int d0 = 0; d0 < 4; ++d0) p0 = __builtin_amdgcn_mfma_f32_32x32x16_bf16(kf[d0], qf[8 + d0], p0, 0, 0, 0);
; #pragma unroll
;     for (int r = 0; r < 16; ++r) sc[r] = fmaf(w[1], relu_i(p1[r]), sc[r]);
;     p1 = f32x16{};
; #pragma unroll
;     for (int d0 = 0; d0 < 4; ++d0) p1 = __builtin_amdgcn_mfma_f32_32x32x16_bf16(kf[d0], qf[12 + d0], p1, 0, 0, 0);
; #pragma unroll
;     for (int r = 0; r < 16; ++r) sc[r] = fmaf(w[2], relu_i(p0[r]), sc[r]);
; #pragma unroll
;     for (int r = 0; r < 16; ++r) sc[r] = fmaf(w[3], relu_i(p1[r]), sc[r]);
; }
; template <int PASS> __device__ __forceinline__ void idx_pass(const bf16_t* KIb, const bf16x8 (&qf)[16], const f32x4& w, int jd, int tq, int wid, int r32, int hi, unsigned khi, unsigned klo, bool cand, LAS unsigned char* L) {
;     ...
;     for (; j <= jd; j += 8) {
;         const bool diag = (j == jd);
;         idx_loadk(kB, KIb + (size_t)(j * 64 + 32) * 64, r32, hi);
;         f32x16 sc; idx_scores_k(sc, kA, qf, w);
;         unsigned lo, elo, hw, ehw;
;         if (diag) idx_half<PASS, true>(lo, elo, sc, j * 64, tq, r32, hi, khi, klo, cand, L); else idx_half<PASS, false>(lo, elo, sc, j * 64, tq, r32, hi, khi, klo, cand, L);
;         if (j + 8 <= jd) idx_loadk(kA, KIb + (size_t)((j + 8) * 64) * 64, r32, hi);
.LBB0_712:
	s_add_i32 s0, s21, s20
	s_cmp_lg_u32 s0, 8
	s_cselect_b64 s[14:15], -1, 0
	s_add_i32 s0, s10, 0xfffffe20
	s_ashr_i32 s1, s0, 31
	s_lshl_b64 s[0:1], s[0:1], 7
	v_lshl_add_u64 v[2:3], v[50:51], 0, s[0:1]
	global_load_dwordx4 v[46:49], v[2:3], off
	global_load_dwordx4 v[42:45], v[2:3], off offset:32
	global_load_dwordx4 v[38:41], v[2:3], off offset:64
	global_load_dwordx4 v[34:37], v[2:3], off offset:96
	s_and_b64 vcc, exec, s[14:15]
	s_waitcnt vmcnt(7) lgkmcnt(14)
	v_mfma_f32_32x32x16_bf16 v[2:17], v[18:21], v[70:73], 0
	s_waitcnt vmcnt(6)
	v_mfma_f32_32x32x16_bf16 v[2:17], v[22:25], v[74:77], v[2:17]
	s_waitcnt vmcnt(5) lgkmcnt(13)
	v_mfma_f32_32x32x16_bf16 v[2:17], v[26:29], v[78:81], v[2:17]
	s_waitcnt vmcnt(4) lgkmcnt(12)
	v_mfma_f32_32x32x16_bf16 v[2:17], v[30:33], v[82:85], v[2:17]
	s_waitcnt lgkmcnt(11)
	v_mfma_f32_32x32x16_bf16 v[180:195], v[18:21], v[86:89], 0
	s_waitcnt lgkmcnt(10)
	v_mfma_f32_32x32x16_bf16 v[180:195], v[22:25], v[90:93], v[180:195]
	s_waitcnt lgkmcnt(9)
	v_mfma_f32_32x32x16_bf16 v[180:195], v[26:29], v[94:97], v[180:195]
	s_waitcnt lgkmcnt(8)
	v_mfma_f32_32x32x16_bf16 v[180:195], v[30:33], v[98:101], v[180:195]
	s_nop 3
	v_max_i32_e32 v196, 0, v2
	v_mul_f32_e32 v136, v66, v196
	v_max_i32_e32 v196, 0, v3
	v_mul_f32_e32 v135, v66, v196
	v_max_i32_e32 v196, 0, v4
	v_mul_f32_e32 v134, v66, v196
	v_max_i32_e32 v196, 0, v5
	v_mul_f32_e32 v65, v66, v196
	v_max_i32_e32 v196, 0, v6
	v_mul_f32_e32 v64, v66, v196
	v_max_i32_e32 v196, 0, v7
	v_mul_f32_e32 v63, v66, v196
	v_max_i32_e32 v196, 0, v8
	v_mul_f32_e32 v62, v66, v196
	v_max_i32_e32 v196, 0, v9
	v_mul_f32_e32 v61, v66, v196
	v_max_i32_e32 v196, 0, v10
	v_mul_f32_e32 v60, v66, v196
	v_max_i32_e32 v196, 0, v11
	v_mul_f32_e32 v59, v66, v196
	v_max_i32_e32 v196, 0, v12
	v_mul_f32_e32 v58, v66, v196
	v_max_i32_e32 v196, 0, v13
	v_mul_f32_e32 v57, v66, v196
	v_max_i32_e32 v196, 0, v14
	v_mul_f32_e32 v56, v66, v196
	v_max_i32_e32 v196, 0, v15
	v_mul_f32_e32 v55, v66, v196
	v_max_i32_e32 v196, 0, v16
	v_mul_f32_e32 v54, v66, v196
	v_max_i32_e32 v196, 0, v17
	v_mul_f32_e32 v53, v66, v196
	s_waitcnt lgkmcnt(7)
	v_mfma_f32_32x32x16_bf16 v[2:17], v[18:21], v[102:105], 0
	s_waitcnt lgkmcnt(6)
	v_mfma_f32_32x32x16_bf16 v[2:17], v[22:25], v[106:109], v[2:17]
	s_waitcnt lgkmcnt(5)
	v_mfma_f32_32x32x16_bf16 v[2:17], v[26:29], v[110:113], v[2:17]
	s_waitcnt lgkmcnt(4)
	v_mfma_f32_32x32x16_bf16 v[2:17], v[30:33], v[114:117], v[2:17]
	v_max_i32_e32 v196, 0, v180
	v_fmac_f32_e32 v136, v67, v196
	v_max_i32_e32 v196, 0, v181
	v_fmac_f32_e32 v135, v67, v196
	v_max_i32_e32 v196, 0, v182
	v_fmac_f32_e32 v134, v67, v196
	v_max_i32_e32 v196, 0, v183
	v_fmac_f32_e32 v65, v67, v196
	v_max_i32_e32 v196, 0, v184
	v_fmac_f32_e32 v64, v67, v196
	v_max_i32_e32 v196, 0, v185
	v_fmac_f32_e32 v63, v67, v196
	v_max_i32_e32 v196, 0, v186
	v_fmac_f32_e32 v62, v67, v196
	v_max_i32_e32 v196, 0, v187
	v_fmac_f32_e32 v61, v67, v196
	v_max_i32_e32 v196, 0, v188
	v_fmac_f32_e32 v60, v67, v196
	v_max_i32_e32 v196, 0, v189
	v_fmac_f32_e32 v59, v67, v196
	v_max_i32_e32 v196, 0, v190
	v_fmac_f32_e32 v58, v67, v196
	v_max_i32_e32 v196, 0, v191
	v_fmac_f32_e32 v57, v67, v196
	v_max_i32_e32 v196, 0, v192
	v_fmac_f32_e32 v56, v67, v196
	v_max_i32_e32 v196, 0, v193
	v_fmac_f32_e32 v55, v67, v196
	v_max_i32_e32 v196, 0, v194
	v_fmac_f32_e32 v54, v67, v196
	v_max_i32_e32 v196, 0, v195
	v_fmac_f32_e32 v53, v67, v196
	s_waitcnt lgkmcnt(3)
	v_mfma_f32_32x32x16_bf16 v[180:195], v[18:21], v[118:121], 0
	s_waitcnt lgkmcnt(2)
	v_mfma_f32_32x32x16_bf16 v[180:195], v[22:25], v[122:125], v[180:195]
	s_waitcnt lgkmcnt(1)
	v_mfma_f32_32x32x16_bf16 v[180:195], v[26:29], v[126:129], v[180:195]
	s_waitcnt lgkmcnt(0)
	v_mfma_f32_32x32x16_bf16 v[180:195], v[30:33], v[130:133], v[180:195]
	v_max_i32_e32 v196, 0, v2
	v_fmac_f32_e32 v136, v68, v196
	v_max_i32_e32 v196, 0, v3
	v_fmac_f32_e32 v135, v68, v196
	v_max_i32_e32 v196, 0, v4
	v_fmac_f32_e32 v134, v68, v196
	v_max_i32_e32 v196, 0, v5
	v_fmac_f32_e32 v65, v68, v196
	v_max_i32_e32 v196, 0, v6
	v_fmac_f32_e32 v64, v68, v196
	v_max_i32_e32 v196, 0, v7
	v_fmac_f32_e32 v63, v68, v196
	v_max_i32_e32 v196, 0, v8
	v_fmac_f32_e32 v62, v68, v196
	v_max_i32_e32 v196, 0, v9
	v_fmac_f32_e32 v61, v68, v196
	v_max_i32_e32 v196, 0, v10
	v_fmac_f32_e32 v60, v68, v196
	v_max_i32_e32 v196, 0, v11
	v_fmac_f32_e32 v59, v68, v196
	v_max_i32_e32 v196, 0, v12
	v_fmac_f32_e32 v58, v68, v196
	v_max_i32_e32 v196, 0, v13
	v_fmac_f32_e32 v57, v68, v196
	v_max_i32_e32 v196, 0, v14
	v_fmac_f32_e32 v56, v68, v196
	v_max_i32_e32 v196, 0, v15
	v_fmac_f32_e32 v55, v68, v196
	v_max_i32_e32 v196, 0, v16
	v_fmac_f32_e32 v54, v68, v196
	v_max_i32_e32 v196, 0, v17
	v_fmac_f32_e32 v53, v68, v196
	v_max_i32_e32 v196, 0, v180
	v_fmac_f32_e32 v136, v69, v196
	v_max_i32_e32 v196, 0, v181
	v_fmac_f32_e32 v135, v69, v196
	v_max_i32_e32 v196, 0, v182
	v_fmac_f32_e32 v134, v69, v196
	v_max_i32_e32 v196, 0, v183
	v_fmac_f32_e32 v65, v69, v196
	v_max_i32_e32 v196, 0, v184
	v_fmac_f32_e32 v64, v69, v196
	v_max_i32_e32 v196, 0, v185
	v_fmac_f32_e32 v63, v69, v196
	v_max_i32_e32 v196, 0, v186
	v_fmac_f32_e32 v62, v69, v196
	v_max_i32_e32 v196, 0, v187
	v_fmac_f32_e32 v61, v69, v196
	v_max_i32_e32 v196, 0, v188
	v_fmac_f32_e32 v60, v69, v196
	v_max_i32_e32 v196, 0, v189
	v_fmac_f32_e32 v59, v69, v196
	v_max_i32_e32 v196, 0, v190
	v_fmac_f32_e32 v58, v69, v196
	v_max_i32_e32 v196, 0, v191
	v_fmac_f32_e32 v57, v69, v196
	v_max_i32_e32 v196, 0, v192
	v_fmac_f32_e32 v56, v69, v196
	v_max_i32_e32 v196, 0, v193
	v_fmac_f32_e32 v55, v69, v196
	v_max_i32_e32 v196, 0, v194
	v_fmac_f32_e32 v54, v69, v196
	v_max_i32_e32 v196, 0, v195
	v_fmac_f32_e32 v53, v69, v196
	s_cbranch_vccz .LBB0_714
; #define LAS __attribute__((address_space(3)))
; __device__ __forceinline__ int crow(int r, int hi) { return (r & 3) + 8 * (r >> 2) + 4 * hi; }
; __device__ __forceinline__ int ibin_u(unsigned u) {
;     const int a = (int)u >> 20;
;     return imed3(-953 - a, 0, 159) + imed3(a - 936, 0, 158) + imed3((int)u, -160, 1) + 160;
; }
; __device__ __forceinline__ int ibin_u_m160(unsigned u) {
;     const int a = (int)u >> 20;
;     return imed3(-953 - a, 0, 159) + imed3(a - 936, 0, 158) + imed3((int)u, -160, 1);
; }
; template <int PASS, bool DIAG> __device__ __forceinline__ void idx_half(unsigned& bits, unsigned& ebits, const f32x16& sc, int sbase, int tq, int r32, int hi, unsigned khi, unsigned klo, bool cand, LAS unsigned char* L) {
;     ...
;         LAS unsigned* H = (LAS unsigned*)(L + IL_HIST) + r32 * HSTR + 160;
; #pragma unroll
;         for (int r = 0; r < 16; ++r) { int b = ibin_u_m160(__float_as_uint(sc[r] + 0.0f)); asm("" : "+v"(b));
;             if (!DIAG || crow(r, 0) <= d) __hip_atomic_fetch_add(H + b, 1u, __ATOMIC_RELAXED, __HIP_MEMORY_SCOPE_WORKGROUP); }
	v_add_f32_e32 v2, 0, v136
	v_ashrrev_i32_e32 v3, 20, v2
	v_sub_u32_e32 v4, 0xfffffc47, v3
	v_med3_i32 v3, v3, s88, v233
	v_med3_i32 v2, v2, s89, 1
	v_med3_i32 v4, v4, 0, v232
	v_add_u32_e32 v2, v2, v3
	v_add3_u32 v2, v2, v4, s92
	s_nop 0
	v_lshl_add_u32 v2, v2, 2, v0
	ds_add_u32 v2, v229 offset:1152
	v_add_f32_e32 v2, 0, v135
	v_ashrrev_i32_e32 v3, 20, v2
	v_sub_u32_e32 v4, 0xfffffc47, v3
	v_med3_i32 v3, v3, s88, v233
	v_med3_i32 v2, v2, s89, 1
	v_med3_i32 v4, v4, 0, v232
	v_add_u32_e32 v2, v2, v3
	v_add3_u32 v2, v2, v4, s92
	s_mov_b64 s[16:17], -1
	v_lshl_add_u32 v2, v2, 2, v0
	ds_add_u32 v2, v229 offset:1152
	v_add_f32_e32 v2, 0, v134
	v_ashrrev_i32_e32 v3, 20, v2
	v_sub_u32_e32 v4, 0xfffffc47, v3
	v_med3_i32 v3, v3, s88, v233
	v_med3_i32 v2, v2, s89, 1
	v_med3_i32 v4, v4, 0, v232
	v_add_u32_e32 v2, v2, v3
	v_add3_u32 v2, v2, v4, s92
	s_nop 0
	v_lshl_add_u32 v2, v2, 2, v0
	ds_add_u32 v2, v229 offset:1152
	v_add_f32_e32 v2, 0, v65
	v_ashrrev_i32_e32 v3, 20, v2
	v_sub_u32_e32 v4, 0xfffffc47, v3
	v_med3_i32 v3, v3, s88, v233
	v_med3_i32 v2, v2, s89, 1
	v_med3_i32 v4, v4, 0, v232
	v_add_u32_e32 v2, v2, v3
	v_add3_u32 v2, v2, v4, s92
	s_nop 0
	v_lshl_add_u32 v2, v2, 2, v0
	ds_add_u32 v2, v229 offset:1152
	v_add_f32_e32 v2, 0, v64
	v_ashrrev_i32_e32 v3, 20, v2
	v_sub_u32_e32 v4, 0xfffffc47, v3
	v_med3_i32 v3, v3, s88, v233
	v_med3_i32 v2, v2, s89, 1
	v_med3_i32 v4, v4, 0, v232
	v_add_u32_e32 v2, v2, v3
	v_add3_u32 v2, v2, v4, s92
	s_nop 0
	v_lshl_add_u32 v2, v2, 2, v0
	ds_add_u32 v2, v229 offset:1152
	v_add_f32_e32 v2, 0, v63
	v_ashrrev_i32_e32 v3, 20, v2
	v_sub_u32_e32 v4, 0xfffffc47, v3
	v_med3_i32 v3, v3, s88, v233
	v_med3_i32 v2, v2, s89, 1
	v_med3_i32 v4, v4, 0, v232
	v_add_u32_e32 v2, v2, v3
	v_add3_u32 v2, v2, v4, s92
	s_nop 0
	v_lshl_add_u32 v2, v2, 2, v0
	ds_add_u32 v2, v229 offset:1152
	v_add_f32_e32 v2, 0, v62
	v_ashrrev_i32_e32 v3, 20, v2
	v_sub_u32_e32 v4, 0xfffffc47, v3
	v_med3_i32 v3, v3, s88, v233
	v_med3_i32 v2, v2, s89, 1
	v_med3_i32 v4, v4, 0, v232
	v_add_u32_e32 v2, v2, v3
	v_add3_u32 v2, v2, v4, s92
	s_nop 0
	v_lshl_add_u32 v2, v2, 2, v0
	ds_add_u32 v2, v229 offset:1152
	v_add_f32_e32 v2, 0, v61
	v_ashrrev_i32_e32 v3, 20, v2
	v_sub_u32_e32 v4, 0xfffffc47, v3
	v_med3_i32 v3, v3, s88, v233
	v_med3_i32 v2, v2, s89, 1
	v_med3_i32 v4, v4, 0, v232
	v_add_u32_e32 v2, v2, v3
	v_add3_u32 v2, v2, v4, s92
	s_nop 0
	v_lshl_add_u32 v2, v2, 2, v0
	ds_add_u32 v2, v229 offset:1152
	v_add_f32_e32 v2, 0, v60
	v_ashrrev_i32_e32 v3, 20, v2
	v_sub_u32_e32 v4, 0xfffffc47, v3
	v_med3_i32 v3, v3, s88, v233
	v_med3_i32 v2, v2, s89, 1
	v_med3_i32 v4, v4, 0, v232
	v_add_u32_e32 v2, v2, v3
	v_add3_u32 v2, v2, v4, s92
	s_nop 0
	v_lshl_add_u32 v2, v2, 2, v0
	ds_add_u32 v2, v229 offset:1152
	v_add_f32_e32 v2, 0, v59
	v_ashrrev_i32_e32 v3, 20, v2
	v_sub_u32_e32 v4, 0xfffffc47, v3
	v_med3_i32 v3, v3, s88, v233
	v_med3_i32 v2, v2, s89, 1
	v_med3_i32 v4, v4, 0, v232
	v_add_u32_e32 v2, v2, v3
	v_add3_u32 v2, v2, v4, s92
	s_nop 0
	v_lshl_add_u32 v2, v2, 2, v0
	ds_add_u32 v2, v229 offset:1152
	v_add_f32_e32 v2, 0, v58
	v_ashrrev_i32_e32 v3, 20, v2
	v_sub_u32_e32 v4, 0xfffffc47, v3
	v_med3_i32 v3, v3, s88, v233
	v_med3_i32 v2, v2, s89, 1
	v_med3_i32 v4, v4, 0, v232
	v_add_u32_e32 v2, v2, v3
	v_add3_u32 v2, v2, v4, s92
	s_nop 0
	v_lshl_add_u32 v2, v2, 2, v0
	ds_add_u32 v2, v229 offset:1152
	v_add_f32_e32 v2, 0, v57
	v_ashrrev_i32_e32 v3, 20, v2
	v_sub_u32_e32 v4, 0xfffffc47, v3
	v_med3_i32 v3, v3, s88, v233
	v_med3_i32 v2, v2, s89, 1
	v_med3_i32 v4, v4, 0, v232
	v_add_u32_e32 v2, v2, v3
	v_add3_u32 v2, v2, v4, s92
	s_nop 0
	v_lshl_add_u32 v2, v2, 2, v0
	ds_add_u32 v2, v229 offset:1152
	v_add_f32_e32 v2, 0, v56
	v_ashrrev_i32_e32 v3, 20, v2
	v_sub_u32_e32 v4, 0xfffffc47, v3
	v_med3_i32 v3, v3, s88, v233
	v_med3_i32 v2, v2, s89, 1
	v_med3_i32 v4, v4, 0, v232
	v_add_u32_e32 v2, v2, v3
	v_add3_u32 v2, v2, v4, s92
	s_nop 0
	v_lshl_add_u32 v2, v2, 2, v0
	ds_add_u32 v2, v229 offset:1152
	v_add_f32_e32 v2, 0, v55
	v_ashrrev_i32_e32 v3, 20, v2
	v_sub_u32_e32 v4, 0xfffffc47, v3
	v_med3_i32 v3, v3, s88, v233
	v_med3_i32 v2, v2, s89, 1
	v_med3_i32 v4, v4, 0, v232
	v_add_u32_e32 v2, v2, v3
	v_add3_u32 v2, v2, v4, s92
	s_nop 0
	v_lshl_add_u32 v2, v2, 2, v0
	ds_add_u32 v2, v229 offset:1152
	v_add_f32_e32 v2, 0, v54
	v_ashrrev_i32_e32 v3, 20, v2
	v_sub_u32_e32 v4, 0xfffffc47, v3
	v_med3_i32 v3, v3, s88, v233
	v_med3_i32 v2, v2, s89, 1
	v_med3_i32 v4, v4, 0, v232
	v_add_u32_e32 v2, v2, v3
	v_add3_u32 v2, v2, v4, s92
	s_nop 0
	v_lshl_add_u32 v2, v2, 2, v0
	ds_add_u32 v2, v229 offset:1152
	v_add_f32_e32 v2, 0, v53
	v_ashrrev_i32_e32 v3, 20, v2
	v_sub_u32_e32 v4, 0xfffffc47, v3
	v_med3_i32 v3, v3, s88, v233
	v_med3_i32 v2, v2, s89, 1
	v_med3_i32 v4, v4, 0, v232
	v_add_u32_e32 v2, v2, v3
	v_add3_u32 v2, v2, v4, s92
	s_cbranch_execz .LBB0_715
	s_branch .LBB0_746

; __device__ __forceinline__ float relu_i(float p) { const int i = __float_as_int(p); return __int_as_float(i > 0 ? i : 0); }
; __device__ __forceinline__ void idx_scores_k(f32x16& sc, const bf16x8 (&kf)[4], const bf16x8 (&qf)[16], const f32x4& w) {
;     f32x16 p0 = f32x16{}, p1 = f32x16{};
; #pragma unroll
;     for (int d0 = 0; d0 < 4; ++d0) p0 = __builtin_amdgcn_mfma_f32_32x32x16_bf16(kf[d0], qf[d0], p0, 0, 0, 0);
; #pragma unroll
;     for (int d0 = 0; d0 < 4; ++d0) p1 = __builtin_amdgcn_mfma_f32_32x32x16_bf16(kf[d0], qf[4 + d0], p1, 0, 0, 0);
; #pragma unroll
;     for (int r = 0; r < 16; ++r) sc[r] = w[0] * relu_i(p0[r]);
;     p0 = f32x16{};
; #pragma unroll
;     for (int d0 = 0; d0 < 4; ++d0) p0 = __builtin_amdgcn_mfma_f32_32x32x16_bf16(kf[d0], qf[8 + d0], p0, 0, 0, 0);
; #pragma unroll
;     for (int r = 0; r < 16; ++r) sc[r] = fmaf(w[1], relu_i(p1[r]), sc[r]);
;     p1 = f32x16{};
; #pragma unroll
;     for (int d0 = 0; d0 < 4; ++d0) p1 = __builtin_amdgcn_mfma_f32_32x32x16_bf16(kf[d0], qf[12 + d0], p1, 0, 0, 0);
; #pragma unroll
;     for (int r = 0; r < 16; ++r) sc[r] = fmaf(w[2], relu_i(p0[r]), sc[r]);
; #pragma unroll
;     for (int r = 0; r < 16; ++r) sc[r] = fmaf(w[3], relu_i(p1[r]), sc[r]);
; }
; template <int PASS> __device__ __forceinline__ void idx_pass(const bf16_t* KIb, const bf16x8 (&qf)[16], const f32x4& w, int jd, int tq, int wid, int r32, int hi, unsigned khi, unsigned klo, bool cand, LAS unsigned char* L) {
;     ...
;         idx_scores_k(sc, kB, qf, w);
.LBB0_750:
	s_and_b64 vcc, exec, s[14:15]
	s_waitcnt vmcnt(3)
	v_mfma_f32_32x32x16_bf16 v[2:17], v[46:49], v[70:73], 0
	s_waitcnt vmcnt(2)
	v_mfma_f32_32x32x16_bf16 v[2:17], v[42:45], v[74:77], v[2:17]
	s_waitcnt vmcnt(1)
	v_mfma_f32_32x32x16_bf16 v[2:17], v[38:41], v[78:81], v[2:17]
	s_waitcnt vmcnt(0)
	v_mfma_f32_32x32x16_bf16 v[2:17], v[34:37], v[82:85], v[2:17]
	v_mfma_f32_32x32x16_bf16 v[180:195], v[46:49], v[86:89], 0
	v_mfma_f32_32x32x16_bf16 v[180:195], v[42:45], v[90:93], v[180:195]
	v_mfma_f32_32x32x16_bf16 v[180:195], v[38:41], v[94:97], v[180:195]
	v_mfma_f32_32x32x16_bf16 v[180:195], v[34:37], v[98:101], v[180:195]
	s_nop 7
	v_max_i32_e32 v196, 0, v2
	v_mul_f32_e32 v136, v66, v196
	v_max_i32_e32 v196, 0, v3
	v_mul_f32_e32 v135, v66, v196
	v_max_i32_e32 v196, 0, v4
	v_mul_f32_e32 v134, v66, v196
	v_max_i32_e32 v196, 0, v5
	v_mul_f32_e32 v65, v66, v196
	v_max_i32_e32 v196, 0, v6
	v_mul_f32_e32 v64, v66, v196
	v_max_i32_e32 v196, 0, v7
	v_mul_f32_e32 v63, v66, v196
	v_max_i32_e32 v196, 0, v8
	v_mul_f32_e32 v62, v66, v196
	v_max_i32_e32 v196, 0, v9
	v_mul_f32_e32 v61, v66, v196
	v_max_i32_e32 v196, 0, v10
	v_mul_f32_e32 v60, v66, v196
	v_max_i32_e32 v196, 0, v11
	v_mul_f32_e32 v59, v66, v196
	v_max_i32_e32 v196, 0, v12
	v_mul_f32_e32 v58, v66, v196
	v_max_i32_e32 v196, 0, v13
	v_mul_f32_e32 v57, v66, v196
	v_max_i32_e32 v196, 0, v14
	v_mul_f32_e32 v56, v66, v196
	v_max_i32_e32 v196, 0, v15
	v_mul_f32_e32 v55, v66, v196
	v_max_i32_e32 v196, 0, v16
	v_mul_f32_e32 v54, v66, v196
	v_max_i32_e32 v196, 0, v17
	v_mul_f32_e32 v53, v66, v196
	v_mfma_f32_32x32x16_bf16 v[2:17], v[46:49], v[102:105], 0
	v_mfma_f32_32x32x16_bf16 v[2:17], v[42:45], v[106:109], v[2:17]
	v_mfma_f32_32x32x16_bf16 v[2:17], v[38:41], v[110:113], v[2:17]
	v_mfma_f32_32x32x16_bf16 v[2:17], v[34:37], v[114:117], v[2:17]
	v_max_i32_e32 v196, 0, v180
	v_fmac_f32_e32 v136, v67, v196
	v_max_i32_e32 v196, 0, v181
	v_fmac_f32_e32 v135, v67, v196
	v_max_i32_e32 v196, 0, v182
	v_fmac_f32_e32 v134, v67, v196
	v_max_i32_e32 v196, 0, v183
	v_fmac_f32_e32 v65, v67, v196
	v_max_i32_e32 v196, 0, v184
	v_fmac_f32_e32 v64, v67, v196
	v_max_i32_e32 v196, 0, v185
	v_fmac_f32_e32 v63, v67, v196
	v_max_i32_e32 v196, 0, v186
	v_fmac_f32_e32 v62, v67, v196
	v_max_i32_e32 v196, 0, v187
	v_fmac_f32_e32 v61, v67, v196
	v_max_i32_e32 v196, 0, v188
	v_fmac_f32_e32 v60, v67, v196
	v_max_i32_e32 v196, 0, v189
	v_fmac_f32_e32 v59, v67, v196
	v_max_i32_e32 v196, 0, v190
	v_fmac_f32_e32 v58, v67, v196
	v_max_i32_e32 v196, 0, v191
	v_fmac_f32_e32 v57, v67, v196
	v_max_i32_e32 v196, 0, v192
	v_fmac_f32_e32 v56, v67, v196
	v_max_i32_e32 v196, 0, v193
	v_fmac_f32_e32 v55, v67, v196
	v_max_i32_e32 v196, 0, v194
	v_fmac_f32_e32 v54, v67, v196
	v_max_i32_e32 v196, 0, v195
	v_fmac_f32_e32 v53, v67, v196
	v_mfma_f32_32x32x16_bf16 v[180:195], v[46:49], v[118:121], 0
	v_mfma_f32_32x32x16_bf16 v[180:195], v[42:45], v[122:125], v[180:195]
	v_mfma_f32_32x32x16_bf16 v[180:195], v[38:41], v[126:129], v[180:195]
	v_mfma_f32_32x32x16_bf16 v[180:195], v[34:37], v[130:133], v[180:195]
	v_max_i32_e32 v196, 0, v2
	v_fmac_f32_e32 v136, v68, v196
	v_max_i32_e32 v196, 0, v3
	v_fmac_f32_e32 v135, v68, v196
	v_max_i32_e32 v196, 0, v4
	v_fmac_f32_e32 v134, v68, v196
	v_max_i32_e32 v196, 0, v5
	v_fmac_f32_e32 v65, v68, v196
	v_max_i32_e32 v196, 0, v6
	v_fmac_f32_e32 v64, v68, v196
	v_max_i32_e32 v196, 0, v7
	v_fmac_f32_e32 v63, v68, v196
	v_max_i32_e32 v196, 0, v8
	v_fmac_f32_e32 v62, v68, v196
	v_max_i32_e32 v196, 0, v9
	v_fmac_f32_e32 v61, v68, v196
	v_max_i32_e32 v196, 0, v10
	v_fmac_f32_e32 v60, v68, v196
	v_max_i32_e32 v196, 0, v11
	v_fmac_f32_e32 v59, v68, v196
	v_max_i32_e32 v196, 0, v12
	v_fmac_f32_e32 v58, v68, v196
	v_max_i32_e32 v196, 0, v13
	v_fmac_f32_e32 v57, v68, v196
	v_max_i32_e32 v196, 0, v14
	v_fmac_f32_e32 v56, v68, v196
	v_max_i32_e32 v196, 0, v15
	v_fmac_f32_e32 v55, v68, v196
	v_max_i32_e32 v196, 0, v16
	v_fmac_f32_e32 v54, v68, v196
	v_max_i32_e32 v196, 0, v17
	v_fmac_f32_e32 v53, v68, v196
	v_max_i32_e32 v196, 0, v180
	v_fmac_f32_e32 v136, v69, v196
	v_max_i32_e32 v196, 0, v181
	v_fmac_f32_e32 v135, v69, v196
	v_max_i32_e32 v196, 0, v182
	v_fmac_f32_e32 v134, v69, v196
	v_max_i32_e32 v196, 0, v183
	v_fmac_f32_e32 v65, v69, v196
	v_max_i32_e32 v196, 0, v184
	v_fmac_f32_e32 v64, v69, v196
	v_max_i32_e32 v196, 0, v185
	v_fmac_f32_e32 v63, v69, v196
	v_max_i32_e32 v196, 0, v186
	v_fmac_f32_e32 v62, v69, v196
	v_max_i32_e32 v196, 0, v187
	v_fmac_f32_e32 v61, v69, v196
	v_max_i32_e32 v196, 0, v188
	v_fmac_f32_e32 v60, v69, v196
	v_max_i32_e32 v196, 0, v189
	v_fmac_f32_e32 v59, v69, v196
	v_max_i32_e32 v196, 0, v190
	v_fmac_f32_e32 v58, v69, v196
	v_max_i32_e32 v196, 0, v191
	v_fmac_f32_e32 v57, v69, v196
	v_max_i32_e32 v196, 0, v192
	v_fmac_f32_e32 v56, v69, v196
	v_max_i32_e32 v196, 0, v193
	v_fmac_f32_e32 v55, v69, v196
	v_max_i32_e32 v196, 0, v194
	v_fmac_f32_e32 v54, v69, v196
	v_max_i32_e32 v196, 0, v195
	v_fmac_f32_e32 v53, v69, v196
	s_cbranch_vccz .LBB0_752
; #define LAS __attribute__((address_space(3)))
; __device__ __forceinline__ int crow(int r, int hi) { return (r & 3) + 8 * (r >> 2) + 4 * hi; }
; __device__ __forceinline__ int ibin_u(unsigned u) {
;     const int a = (int)u >> 20;
;     return imed3(-953 - a, 0, 159) + imed3(a - 936, 0, 158) + imed3((int)u, -160, 1) + 160;
; }
; __device__ __forceinline__ int ibin_u_m160(unsigned u) {
;     const int a = (int)u >> 20;
;     return imed3(-953 - a, 0, 159) + imed3(a - 936, 0, 158) + imed3((int)u, -160, 1);
; }
; template <int PASS, bool DIAG> __device__ __forceinline__ void idx_half(unsigned& bits, unsigned& ebits, const f32x16& sc, int sbase, int tq, int r32, int hi, unsigned khi, unsigned klo, bool cand, LAS unsigned char* L) {
;     ...
;         LAS unsigned* H = (LAS unsigned*)(L + IL_HIST) + r32 * HSTR + 160;
; #pragma unroll
;         for (int r = 0; r < 16; ++r) { int b = ibin_u_m160(__float_as_uint(sc[r] + 0.0f)); asm("" : "+v"(b));
;             if (!DIAG || crow(r, 0) <= d) __hip_atomic_fetch_add(H + b, 1u, __ATOMIC_RELAXED, __HIP_MEMORY_SCOPE_WORKGROUP); }
	v_add_f32_e32 v2, 0, v136
	v_ashrrev_i32_e32 v3, 20, v2
	v_sub_u32_e32 v4, 0xfffffc47, v3
	v_med3_i32 v3, v3, s88, v233
	v_med3_i32 v2, v2, s89, 1
	v_med3_i32 v4, v4, 0, v232
	v_add_u32_e32 v2, v2, v3
	v_add3_u32 v2, v2, v4, s92
	s_nop 0
	v_lshl_add_u32 v2, v2, 2, v0
	ds_add_u32 v2, v229 offset:1152
	v_add_f32_e32 v2, 0, v135
	v_ashrrev_i32_e32 v3, 20, v2
	v_sub_u32_e32 v4, 0xfffffc47, v3
	v_med3_i32 v3, v3, s88, v233
	v_med3_i32 v2, v2, s89, 1
	v_med3_i32 v4, v4, 0, v232
	v_add_u32_e32 v2, v2, v3
	v_add3_u32 v2, v2, v4, s92
	s_mov_b64 s[14:15], -1
	v_lshl_add_u32 v2, v2, 2, v0
	ds_add_u32 v2, v229 offset:1152
	v_add_f32_e32 v2, 0, v134
	v_ashrrev_i32_e32 v3, 20, v2
	v_sub_u32_e32 v4, 0xfffffc47, v3
	v_med3_i32 v3, v3, s88, v233
	v_med3_i32 v2, v2, s89, 1
	v_med3_i32 v4, v4, 0, v232
	v_add_u32_e32 v2, v2, v3
	v_add3_u32 v2, v2, v4, s92
	s_nop 0
	v_lshl_add_u32 v2, v2, 2, v0
	ds_add_u32 v2, v229 offset:1152
	v_add_f32_e32 v2, 0, v65
	v_ashrrev_i32_e32 v3, 20, v2
	v_sub_u32_e32 v4, 0xfffffc47, v3
	v_med3_i32 v3, v3, s88, v233
	v_med3_i32 v2, v2, s89, 1
	v_med3_i32 v4, v4, 0, v232
	v_add_u32_e32 v2, v2, v3
	v_add3_u32 v2, v2, v4, s92
	s_nop 0
	v_lshl_add_u32 v2, v2, 2, v0
	ds_add_u32 v2, v229 offset:1152
	v_add_f32_e32 v2, 0, v64
	v_ashrrev_i32_e32 v3, 20, v2
	v_sub_u32_e32 v4, 0xfffffc47, v3
	v_med3_i32 v3, v3, s88, v233
	v_med3_i32 v2, v2, s89, 1
	v_med3_i32 v4, v4, 0, v232
	v_add_u32_e32 v2, v2, v3
	v_add3_u32 v2, v2, v4, s92
	s_nop 0
	v_lshl_add_u32 v2, v2, 2, v0
	ds_add_u32 v2, v229 offset:1152
	v_add_f32_e32 v2, 0, v63
	v_ashrrev_i32_e32 v3, 20, v2
	v_sub_u32_e32 v4, 0xfffffc47, v3
	v_med3_i32 v3, v3, s88, v233
	v_med3_i32 v2, v2, s89, 1
	v_med3_i32 v4, v4, 0, v232
	v_add_u32_e32 v2, v2, v3
	v_add3_u32 v2, v2, v4, s92
	s_nop 0
	v_lshl_add_u32 v2, v2, 2, v0
	ds_add_u32 v2, v229 offset:1152
	v_add_f32_e32 v2, 0, v62
	v_ashrrev_i32_e32 v3, 20, v2
	v_sub_u32_e32 v4, 0xfffffc47, v3
	v_med3_i32 v3, v3, s88, v233
	v_med3_i32 v2, v2, s89, 1
	v_med3_i32 v4, v4, 0, v232
	v_add_u32_e32 v2, v2, v3
	v_add3_u32 v2, v2, v4, s92
	s_nop 0
	v_lshl_add_u32 v2, v2, 2, v0
	ds_add_u32 v2, v229 offset:1152
	v_add_f32_e32 v2, 0, v61
	v_ashrrev_i32_e32 v3, 20, v2
	v_sub_u32_e32 v4, 0xfffffc47, v3
	v_med3_i32 v3, v3, s88, v233
	v_med3_i32 v2, v2, s89, 1
	v_med3_i32 v4, v4, 0, v232
	v_add_u32_e32 v2, v2, v3
	v_add3_u32 v2, v2, v4, s92
	s_nop 0
	v_lshl_add_u32 v2, v2, 2, v0
	ds_add_u32 v2, v229 offset:1152
	v_add_f32_e32 v2, 0, v60
	v_ashrrev_i32_e32 v3, 20, v2
	v_sub_u32_e32 v4, 0xfffffc47, v3
	v_med3_i32 v3, v3, s88, v233
	v_med3_i32 v2, v2, s89, 1
	v_med3_i32 v4, v4, 0, v232
	v_add_u32_e32 v2, v2, v3
	v_add3_u32 v2, v2, v4, s92
	s_nop 0
	v_lshl_add_u32 v2, v2, 2, v0
	ds_add_u32 v2, v229 offset:1152
	v_add_f32_e32 v2, 0, v59
	v_ashrrev_i32_e32 v3, 20, v2
	v_sub_u32_e32 v4, 0xfffffc47, v3
	v_med3_i32 v3, v3, s88, v233
	v_med3_i32 v2, v2, s89, 1
	v_med3_i32 v4, v4, 0, v232
	v_add_u32_e32 v2, v2, v3
	v_add3_u32 v2, v2, v4, s92
	s_nop 0
	v_lshl_add_u32 v2, v2, 2, v0
	ds_add_u32 v2, v229 offset:1152
	v_add_f32_e32 v2, 0, v58
	v_ashrrev_i32_e32 v3, 20, v2
	v_sub_u32_e32 v4, 0xfffffc47, v3
	v_med3_i32 v3, v3, s88, v233
	v_med3_i32 v2, v2, s89, 1
	v_med3_i32 v4, v4, 0, v232
	v_add_u32_e32 v2, v2, v3
	v_add3_u32 v2, v2, v4, s92
	s_nop 0
	v_lshl_add_u32 v2, v2, 2, v0
	ds_add_u32 v2, v229 offset:1152
	v_add_f32_e32 v2, 0, v57
	v_ashrrev_i32_e32 v3, 20, v2
	v_sub_u32_e32 v4, 0xfffffc47, v3
	v_med3_i32 v3, v3, s88, v233
	v_med3_i32 v2, v2, s89, 1
	v_med3_i32 v4, v4, 0, v232
	v_add_u32_e32 v2, v2, v3
	v_add3_u32 v2, v2, v4, s92
	s_nop 0
	v_lshl_add_u32 v2, v2, 2, v0
	ds_add_u32 v2, v229 offset:1152
	v_add_f32_e32 v2, 0, v56
	v_ashrrev_i32_e32 v3, 20, v2
	v_sub_u32_e32 v4, 0xfffffc47, v3
	v_med3_i32 v3, v3, s88, v233
	v_med3_i32 v2, v2, s89, 1
	v_med3_i32 v4, v4, 0, v232
	v_add_u32_e32 v2, v2, v3
	v_add3_u32 v2, v2, v4, s92
	s_nop 0
	v_lshl_add_u32 v2, v2, 2, v0
	ds_add_u32 v2, v229 offset:1152
	v_add_f32_e32 v2, 0, v55
	v_ashrrev_i32_e32 v3, 20, v2
	v_sub_u32_e32 v4, 0xfffffc47, v3
	v_med3_i32 v3, v3, s88, v233
	v_med3_i32 v2, v2, s89, 1
	v_med3_i32 v4, v4, 0, v232
	v_add_u32_e32 v2, v2, v3
	v_add3_u32 v2, v2, v4, s92
	s_nop 0
	v_lshl_add_u32 v2, v2, 2, v0
	ds_add_u32 v2, v229 offset:1152
	v_add_f32_e32 v2, 0, v54
	v_ashrrev_i32_e32 v3, 20, v2
	v_sub_u32_e32 v4, 0xfffffc47, v3
	v_med3_i32 v3, v3, s88, v233
	v_med3_i32 v2, v2, s89, 1
	v_med3_i32 v4, v4, 0, v232
	v_add_u32_e32 v2, v2, v3
	v_add3_u32 v2, v2, v4, s92
	s_nop 0
	v_lshl_add_u32 v2, v2, 2, v0
	ds_add_u32 v2, v229 offset:1152
	v_add_f32_e32 v2, 0, v53
	v_ashrrev_i32_e32 v3, 20, v2
	v_sub_u32_e32 v4, 0xfffffc47, v3
	v_med3_i32 v3, v3, s88, v233
	v_med3_i32 v2, v2, s89, 1
	v_med3_i32 v4, v4, 0, v232
	v_add_u32_e32 v2, v2, v3
	v_add3_u32 v3, v2, v4, s92
	s_cbranch_execz .LBB0_753
	s_branch .LBB0_784

; __device__ __forceinline__ float relu_i(float p) { const int i = __float_as_int(p); return __int_as_float(i > 0 ? i : 0); }
; __device__ __forceinline__ void idx_scores_k(f32x16& sc, const bf16x8 (&kf)[4], const bf16x8 (&qf)[16], const f32x4& w) {
;     f32x16 p0 = f32x16{}, p1 = f32x16{};
; #pragma unroll
;     for (int d0 = 0; d0 < 4; ++d0) p0 = __builtin_amdgcn_mfma_f32_32x32x16_bf16(kf[d0], qf[d0], p0, 0, 0, 0);
; #pragma unroll
;     for (int d0 = 0; d0 < 4; ++d0) p1 = __builtin_amdgcn_mfma_f32_32x32x16_bf16(kf[d0], qf[4 + d0], p1, 0, 0, 0);
; #pragma unroll
;     for (int r = 0; r < 16; ++r) sc[r] = w[0] * relu_i(p0[r]);
;     p0 = f32x16{};
; #pragma unroll
;     for (int d0 = 0; d0 < 4; ++d0) p0 = __builtin_amdgcn_mfma_f32_32x32x16_bf16(kf[d0], qf[8 + d0], p0, 0, 0, 0);
; #pragma unroll
;     for (int r = 0; r < 16; ++r) sc[r] = fmaf(w[1], relu_i(p1[r]), sc[r]);
;     p1 = f32x16{};
; #pragma unroll
;     for (int d0 = 0; d0 < 4; ++d0) p1 = __builtin_amdgcn_mfma_f32_32x32x16_bf16(kf[d0], qf[12 + d0], p1, 0, 0, 0);
; #pragma unroll
;     for (int r = 0; r < 16; ++r) sc[r] = fmaf(w[2], relu_i(p0[r]), sc[r]);
; #pragma unroll
;     for (int r = 0; r < 16; ++r) sc[r] = fmaf(w[3], relu_i(p1[r]), sc[r]);
; }
; template <int PASS> __device__ __forceinline__ void idx_pass(const bf16_t* KIb, const bf16x8 (&qf)[16], const f32x4& w, int jd, int tq, int wid, int r32, int hi, unsigned khi, unsigned klo, bool cand, LAS unsigned char* L) {
;     ...
;     for (; j <= jd; j += 8) {
;         const bool diag = (j == jd);
;         idx_loadk(kB, KIb + (size_t)(j * 64 + 32) * 64, r32, hi);
;         f32x16 sc; idx_scores_k(sc, kA, qf, w);
;         unsigned lo, elo, hw, ehw;
;         if (diag) idx_half<PASS, true>(lo, elo, sc, j * 64, tq, r32, hi, khi, klo, cand, L); else idx_half<PASS, false>(lo, elo, sc, j * 64, tq, r32, hi, khi, klo, cand, L);
.LBB0_1064:
	s_add_i32 s0, s46, s44
	s_cmp_lg_u32 s0, 8
	s_cselect_b64 s[18:19], -1, 0
	s_add_i32 s0, s16, 0xfffffe20
	s_ashr_i32 s1, s0, 31
	s_lshl_b64 s[0:1], s[0:1], 7
	v_lshl_add_u64 v[2:3], v[50:51], 0, s[0:1]
	global_load_dwordx4 v[46:49], v[2:3], off
	global_load_dwordx4 v[42:45], v[2:3], off offset:32
	global_load_dwordx4 v[38:41], v[2:3], off offset:64
	global_load_dwordx4 v[34:37], v[2:3], off offset:96
	s_mov_b64 s[14:15], -1
	s_and_b64 vcc, exec, s[18:19]
	s_waitcnt vmcnt(7)
	v_mfma_f32_32x32x16_bf16 v[2:17], v[18:21], v[70:73], 0
	s_waitcnt vmcnt(6)
	v_mfma_f32_32x32x16_bf16 v[2:17], v[22:25], v[74:77], v[2:17]
	s_waitcnt vmcnt(5)
	v_mfma_f32_32x32x16_bf16 v[2:17], v[26:29], v[78:81], v[2:17]
	s_waitcnt vmcnt(4)
	v_mfma_f32_32x32x16_bf16 v[2:17], v[30:33], v[82:85], v[2:17]
	v_mfma_f32_32x32x16_bf16 v[180:195], v[18:21], v[86:89], 0
	v_mfma_f32_32x32x16_bf16 v[180:195], v[22:25], v[90:93], v[180:195]
	v_mfma_f32_32x32x16_bf16 v[180:195], v[26:29], v[94:97], v[180:195]
	v_mfma_f32_32x32x16_bf16 v[180:195], v[30:33], v[98:101], v[180:195]
	s_nop 7
	v_max_i32_e32 v196, 0, v2
	v_mul_f32_e32 v144, v66, v196
	v_max_i32_e32 v196, 0, v3
	v_mul_f32_e32 v145, v66, v196
	v_max_i32_e32 v196, 0, v4
	v_mul_f32_e32 v146, v66, v196
	v_max_i32_e32 v196, 0, v5
	v_mul_f32_e32 v147, v66, v196
	v_max_i32_e32 v196, 0, v6
	v_mul_f32_e32 v148, v66, v196
	v_max_i32_e32 v196, 0, v7
	v_mul_f32_e32 v149, v66, v196
	v_max_i32_e32 v196, 0, v8
	v_mul_f32_e32 v150, v66, v196
	v_max_i32_e32 v196, 0, v9
	v_mul_f32_e32 v151, v66, v196
	v_max_i32_e32 v196, 0, v10
	v_mul_f32_e32 v152, v66, v196
	v_max_i32_e32 v196, 0, v11
	v_mul_f32_e32 v153, v66, v196
	v_max_i32_e32 v196, 0, v12
	v_mul_f32_e32 v154, v66, v196
	v_max_i32_e32 v196, 0, v13
	v_mul_f32_e32 v155, v66, v196
	v_max_i32_e32 v196, 0, v14
	v_mul_f32_e32 v156, v66, v196
	v_max_i32_e32 v196, 0, v15
	v_mul_f32_e32 v157, v66, v196
	v_max_i32_e32 v196, 0, v16
	v_mul_f32_e32 v158, v66, v196
	v_max_i32_e32 v196, 0, v17
	v_mul_f32_e32 v159, v66, v196
	v_mfma_f32_32x32x16_bf16 v[2:17], v[18:21], v[102:105], 0
	v_mfma_f32_32x32x16_bf16 v[2:17], v[22:25], v[106:109], v[2:17]
	v_mfma_f32_32x32x16_bf16 v[2:17], v[26:29], v[110:113], v[2:17]
	v_mfma_f32_32x32x16_bf16 v[2:17], v[30:33], v[114:117], v[2:17]
	v_max_i32_e32 v196, 0, v180
	v_fmac_f32_e32 v144, v67, v196
	v_max_i32_e32 v196, 0, v181
	v_fmac_f32_e32 v145, v67, v196
	v_max_i32_e32 v196, 0, v182
	v_fmac_f32_e32 v146, v67, v196
	v_max_i32_e32 v196, 0, v183
	v_fmac_f32_e32 v147, v67, v196
	v_max_i32_e32 v196, 0, v184
	v_fmac_f32_e32 v148, v67, v196
	v_max_i32_e32 v196, 0, v185
	v_fmac_f32_e32 v149, v67, v196
	v_max_i32_e32 v196, 0, v186
	v_fmac_f32_e32 v150, v67, v196
	v_max_i32_e32 v196, 0, v187
	v_fmac_f32_e32 v151, v67, v196
	v_max_i32_e32 v196, 0, v188
	v_fmac_f32_e32 v152, v67, v196
	v_max_i32_e32 v196, 0, v189
	v_fmac_f32_e32 v153, v67, v196
	v_max_i32_e32 v196, 0, v190
	v_fmac_f32_e32 v154, v67, v196
	v_max_i32_e32 v196, 0, v191
	v_fmac_f32_e32 v155, v67, v196
	v_max_i32_e32 v196, 0, v192
	v_fmac_f32_e32 v156, v67, v196
	v_max_i32_e32 v196, 0, v193
	v_fmac_f32_e32 v157, v67, v196
	v_max_i32_e32 v196, 0, v194
	v_fmac_f32_e32 v158, v67, v196
	v_max_i32_e32 v196, 0, v195
	v_fmac_f32_e32 v159, v67, v196
	v_mfma_f32_32x32x16_bf16 v[180:195], v[18:21], v[118:121], 0
	v_mfma_f32_32x32x16_bf16 v[180:195], v[22:25], v[122:125], v[180:195]
	v_mfma_f32_32x32x16_bf16 v[180:195], v[26:29], v[126:129], v[180:195]
	v_mfma_f32_32x32x16_bf16 v[180:195], v[30:33], v[130:133], v[180:195]
	v_max_i32_e32 v196, 0, v2
	v_fmac_f32_e32 v144, v68, v196
	v_max_i32_e32 v196, 0, v3
	v_fmac_f32_e32 v145, v68, v196
	v_max_i32_e32 v196, 0, v4
	v_fmac_f32_e32 v146, v68, v196
	v_max_i32_e32 v196, 0, v5
	v_fmac_f32_e32 v147, v68, v196
	v_max_i32_e32 v196, 0, v6
	v_fmac_f32_e32 v148, v68, v196
	v_max_i32_e32 v196, 0, v7
	v_fmac_f32_e32 v149, v68, v196
	v_max_i32_e32 v196, 0, v8
	v_fmac_f32_e32 v150, v68, v196
	v_max_i32_e32 v196, 0, v9
	v_fmac_f32_e32 v151, v68, v196
	v_max_i32_e32 v196, 0, v10
	v_fmac_f32_e32 v152, v68, v196
	v_max_i32_e32 v196, 0, v11
	v_fmac_f32_e32 v153, v68, v196
	v_max_i32_e32 v196, 0, v12
	v_fmac_f32_e32 v154, v68, v196
	v_max_i32_e32 v196, 0, v13
	v_fmac_f32_e32 v155, v68, v196
	v_max_i32_e32 v196, 0, v14
	v_fmac_f32_e32 v156, v68, v196
	v_max_i32_e32 v196, 0, v15
	v_fmac_f32_e32 v157, v68, v196
	v_max_i32_e32 v196, 0, v16
	v_fmac_f32_e32 v158, v68, v196
	v_max_i32_e32 v196, 0, v17
	v_fmac_f32_e32 v159, v68, v196
	v_max_i32_e32 v196, 0, v180
	v_fmac_f32_e32 v144, v69, v196
	v_max_i32_e32 v196, 0, v181
	v_fmac_f32_e32 v145, v69, v196
	v_max_i32_e32 v196, 0, v182
	v_fmac_f32_e32 v146, v69, v196
	v_max_i32_e32 v196, 0, v183
	v_fmac_f32_e32 v147, v69, v196
	v_max_i32_e32 v196, 0, v184
	v_fmac_f32_e32 v148, v69, v196
	v_max_i32_e32 v196, 0, v185
	v_fmac_f32_e32 v149, v69, v196
	v_max_i32_e32 v196, 0, v186
	v_fmac_f32_e32 v150, v69, v196
	v_max_i32_e32 v196, 0, v187
	v_fmac_f32_e32 v151, v69, v196
	v_max_i32_e32 v196, 0, v188
	v_fmac_f32_e32 v152, v69, v196
	v_max_i32_e32 v196, 0, v189
	v_fmac_f32_e32 v153, v69, v196
	v_max_i32_e32 v196, 0, v190
	v_fmac_f32_e32 v154, v69, v196
	v_max_i32_e32 v196, 0, v191
	v_fmac_f32_e32 v155, v69, v196
	v_max_i32_e32 v196, 0, v192
	v_fmac_f32_e32 v156, v69, v196
	v_max_i32_e32 v196, 0, v193
	v_fmac_f32_e32 v157, v69, v196
	v_max_i32_e32 v196, 0, v194
	v_fmac_f32_e32 v158, v69, v196
	v_max_i32_e32 v196, 0, v195
	v_fmac_f32_e32 v159, v69, v196
	s_cbranch_vccz .LBB0_1263
; #define LAS __attribute__((address_space(3)))
; __device__ __forceinline__ int crow(int r, int hi) { return (r & 3) + 8 * (r >> 2) + 4 * hi; }
; __device__ __forceinline__ unsigned fkey2(float v) { const unsigned u = __float_as_uint(v + 0.0f); return u ^ ((unsigned)((int)u >> 31) | 0x80000000u); }
; __device__ __forceinline__ void shl_ge(unsigned& acc, unsigned key, unsigned thr) { asm("v_cmp_ge_u32 vcc, %1, %2\n\tv_addc_co_u32 %0, vcc, %0, %0, vcc" : "+v"(acc) : "v"(key), "v"(thr) : "vcc"); }
; __device__ __forceinline__ unsigned spread4(unsigned x) { return (x & 0xFu) | ((x & 0xF0u) << 4) | ((x & 0xF00u) << 8) | ((x & 0xF000u) << 12); }
; template <int PASS, bool DIAG> __device__ __forceinline__ void idx_half(unsigned& bits, unsigned& ebits, const f32x16& sc, int sbase, int tq, int r32, int hi, unsigned khi, unsigned klo, bool cand, LAS unsigned char* L) {
;     ...
;         unsigned hb = 0u, lb = 0u;
; #pragma unroll
;         for (int r = 15; r >= 0; --r) { const unsigned key = fkey2(sc[r]); shl_ge(hb, key, khi); shl_ge(lb, key, klo); }
;         bits = spread4(hb); ebits = spread4(lb & ~hb);
;         if (DIAG) { const unsigned vm = d < 0 ? 0u : (d >= 31 ? 0xFFFFFFFFu : ((2u << d) - 1u)); bits &= vm; ebits &= vm; }
;         if (cand && ebits != 0u) {
;             unsigned slot = __hip_atomic_fetch_add((LAS unsigned*)(L + IL_CNT) + r32, (unsigned)__builtin_popcount(ebits), __ATOMIC_RELAXED, __HIP_MEMORY_SCOPE_WORKGROUP);
; #pragma unroll
;             for (int r = 0; r < 16; ++r) if ((ebits >> crow(r, 0)) & 1u) { const int s = sbase + crow(r, hi);
;                 if (slot < (unsigned)IDX_CAP) ((LAS unsigned long long*)(L + IL_CAND))[r32 * IDX_CAP + slot] = ((unsigned long long)fkey2(sc[r]) << 16) | (unsigned long long)(0xFFFFu - (unsigned)s);
;                 ++slot; }
	v_add_f32_e32 v0, 0, v159
	v_ashrrev_i32_e32 v2, 31, v0
	v_bitop3_b32 v2, v2, v0, s85 bitop3:0x36
	v_add_f32_e32 v0, 0, v158
	v_ashrrev_i32_e32 v3, 31, v0
	v_bitop3_b32 v4, v3, v0, s85 bitop3:0x36
	v_add_f32_e32 v0, 0, v157
	v_ashrrev_i32_e32 v3, 31, v0
	v_bitop3_b32 v6, v3, v0, s85 bitop3:0x36
	v_add_f32_e32 v0, 0, v156
	v_ashrrev_i32_e32 v3, 31, v0
	v_bitop3_b32 v8, v3, v0, s85 bitop3:0x36
	v_add_f32_e32 v0, 0, v155
	v_ashrrev_i32_e32 v3, 31, v0
	v_bitop3_b32 v10, v3, v0, s85 bitop3:0x36
	v_add_f32_e32 v0, 0, v154
	v_ashrrev_i32_e32 v3, 31, v0
	v_bitop3_b32 v12, v3, v0, s85 bitop3:0x36
	v_add_f32_e32 v0, 0, v153
	v_ashrrev_i32_e32 v3, 31, v0
	v_bitop3_b32 v14, v3, v0, s85 bitop3:0x36
	v_add_f32_e32 v0, 0, v152
	v_ashrrev_i32_e32 v3, 31, v0
	v_mov_b32_e32 v160, 0
	v_mov_b32_e32 v5, 0
	v_bitop3_b32 v16, v3, v0, s85 bitop3:0x36
	v_add_f32_e32 v0, 0, v151
	v_cmp_ge_u32 vcc, v2, v135
	v_addc_co_u32 v160, vcc, v160, v160, vcc
	v_ashrrev_i32_e32 v3, 31, v0
	v_cmp_ge_u32 vcc, v2, v134
	v_addc_co_u32 v5, vcc, v5, v5, vcc
	v_bitop3_b32 v52, v3, v0, s85 bitop3:0x36
	v_cmp_ge_u32 vcc, v4, v135
	v_addc_co_u32 v160, vcc, v160, v160, vcc
	v_add_f32_e32 v0, 0, v150
	v_cmp_ge_u32 vcc, v4, v134
	v_addc_co_u32 v5, vcc, v5, v5, vcc
	v_ashrrev_i32_e32 v3, 31, v0
	v_cmp_ge_u32 vcc, v6, v135
	v_addc_co_u32 v160, vcc, v160, v160, vcc
	v_bitop3_b32 v54, v3, v0, s85 bitop3:0x36
	v_cmp_ge_u32 vcc, v6, v134
	v_addc_co_u32 v5, vcc, v5, v5, vcc
	v_add_f32_e32 v0, 0, v149
	v_cmp_ge_u32 vcc, v8, v135
	v_addc_co_u32 v160, vcc, v160, v160, vcc
	v_ashrrev_i32_e32 v3, 31, v0
	v_cmp_ge_u32 vcc, v8, v134
	v_addc_co_u32 v5, vcc, v5, v5, vcc
	v_bitop3_b32 v56, v3, v0, s85 bitop3:0x36
	v_cmp_ge_u32 vcc, v10, v135
	v_addc_co_u32 v160, vcc, v160, v160, vcc
	v_add_f32_e32 v0, 0, v148
	v_cmp_ge_u32 vcc, v10, v134
	v_addc_co_u32 v5, vcc, v5, v5, vcc
	v_ashrrev_i32_e32 v3, 31, v0
	v_cmp_ge_u32 vcc, v12, v135
	v_addc_co_u32 v160, vcc, v160, v160, vcc
	v_bitop3_b32 v58, v3, v0, s85 bitop3:0x36
	v_cmp_ge_u32 vcc, v12, v134
	v_addc_co_u32 v5, vcc, v5, v5, vcc
	v_add_f32_e32 v0, 0, v147
	v_cmp_ge_u32 vcc, v14, v135
	v_addc_co_u32 v160, vcc, v160, v160, vcc
	v_ashrrev_i32_e32 v3, 31, v0
	v_cmp_ge_u32 vcc, v14, v134
	v_addc_co_u32 v5, vcc, v5, v5, vcc
	v_bitop3_b32 v60, v3, v0, s85 bitop3:0x36
	v_cmp_ge_u32 vcc, v16, v135
	v_addc_co_u32 v160, vcc, v160, v160, vcc
	v_add_f32_e32 v0, 0, v146
	v_cmp_ge_u32 vcc, v16, v134
	v_addc_co_u32 v5, vcc, v5, v5, vcc
	v_ashrrev_i32_e32 v3, 31, v0
	v_cmp_ge_u32 vcc, v52, v135
	v_addc_co_u32 v160, vcc, v160, v160, vcc
	v_bitop3_b32 v62, v3, v0, s85 bitop3:0x36
	v_cmp_ge_u32 vcc, v52, v134
	v_addc_co_u32 v5, vcc, v5, v5, vcc
	v_add_f32_e32 v0, 0, v145
	v_cmp_ge_u32 vcc, v54, v135
	v_addc_co_u32 v160, vcc, v160, v160, vcc
	v_ashrrev_i32_e32 v3, 31, v0
	v_cmp_ge_u32 vcc, v54, v134
	v_addc_co_u32 v5, vcc, v5, v5, vcc
	v_bitop3_b32 v64, v3, v0, s85 bitop3:0x36
	v_cmp_ge_u32 vcc, v56, v135
	v_addc_co_u32 v160, vcc, v160, v160, vcc
	v_add_f32_e32 v0, 0, v144
	v_cmp_ge_u32 vcc, v56, v134
	v_addc_co_u32 v5, vcc, v5, v5, vcc
	v_ashrrev_i32_e32 v3, 31, v0
	v_cmp_ge_u32 vcc, v58, v135
	v_addc_co_u32 v160, vcc, v160, v160, vcc
	v_bitop3_b32 v0, v3, v0, s85 bitop3:0x36
	v_cmp_ge_u32 vcc, v58, v134
	v_addc_co_u32 v5, vcc, v5, v5, vcc
	s_nop 0
	v_cmp_ge_u32 vcc, v60, v135
	v_addc_co_u32 v160, vcc, v160, v160, vcc
	s_nop 0
	v_cmp_ge_u32 vcc, v60, v134
	v_addc_co_u32 v5, vcc, v5, v5, vcc
	s_nop 0
	v_cmp_ge_u32 vcc, v62, v135
	v_addc_co_u32 v160, vcc, v160, v160, vcc
	s_nop 0
	v_cmp_ge_u32 vcc, v62, v134
	v_addc_co_u32 v5, vcc, v5, v5, vcc
	s_nop 0
	v_cmp_ge_u32 vcc, v64, v135
	v_addc_co_u32 v160, vcc, v160, v160, vcc
	s_nop 0
	v_cmp_ge_u32 vcc, v64, v134
	v_addc_co_u32 v5, vcc, v5, v5, vcc
	s_nop 0
	v_cmp_ge_u32 vcc, v0, v135
	v_addc_co_u32 v160, vcc, v160, v160, vcc
	s_nop 0
	v_cmp_ge_u32 vcc, v0, v134
	v_addc_co_u32 v5, vcc, v5, v5, vcc
	s_nop 0
	v_bitop3_b32 v3, v5, v160, v5 bitop3:0x30
	v_bitop3_b32 v5, v5, 15, v160 bitop3:0x40
	v_lshlrev_b32_e32 v7, 4, v3
	v_and_or_b32 v5, v7, s93, v5
	v_lshlrev_b32_e32 v7, 8, v3
	v_lshlrev_b32_e32 v9, 12, v3
	v_and_b32_e32 v7, 0xf0000, v7
	v_and_b32_e32 v9, 0xf000000, v9
	v_or3_b32 v143, v5, v7, v9
	v_cmp_ne_u32_e32 vcc, 0, v143
	s_and_b64 s[0:1], s[10:11], vcc
	s_and_saveexec_b64 s[20:21], s[0:1]
	s_cbranch_execz .LBB0_1128
	v_bcnt_u32_b32 v5, v143, 0
	ds_add_rtn_u32 v161, v221, v5
	v_and_b32_e32 v5, 1, v3
	v_cmp_eq_u32_e32 vcc, 1, v5
	s_and_saveexec_b64 s[14:15], vcc
	s_cbranch_execz .LBB0_1070
	s_waitcnt lgkmcnt(0)
	v_cmp_gt_u32_e32 vcc, s87, v161
	s_and_saveexec_b64 s[42:43], vcc
	v_lshlrev_b64 v[162:163], 16, v[0:1]
	v_add_u32_e32 v0, s45, v142
	v_lshl_add_u32 v5, v161, 3, v136
	v_or_b32_e32 v162, v162, v0
	ds_write_b64 v5, v[162:163] offset:512
	s_or_b64 exec, exec, s[42:43]
	v_add_u32_e32 v161, 1, v161

; __device__ __forceinline__ float relu_i(float p) { const int i = __float_as_int(p); return __int_as_float(i > 0 ? i : 0); }
; __device__ __forceinline__ void idx_scores_k(f32x16& sc, const bf16x8 (&kf)[4], const bf16x8 (&qf)[16], const f32x4& w) {
;     f32x16 p0 = f32x16{}, p1 = f32x16{};
; #pragma unroll
;     for (int d0 = 0; d0 < 4; ++d0) p0 = __builtin_amdgcn_mfma_f32_32x32x16_bf16(kf[d0], qf[d0], p0, 0, 0, 0);
; #pragma unroll
;     for (int d0 = 0; d0 < 4; ++d0) p1 = __builtin_amdgcn_mfma_f32_32x32x16_bf16(kf[d0], qf[4 + d0], p1, 0, 0, 0);
; #pragma unroll
;     for (int r = 0; r < 16; ++r) sc[r] = w[0] * relu_i(p0[r]);
;     p0 = f32x16{};
; #pragma unroll
;     for (int d0 = 0; d0 < 4; ++d0) p0 = __builtin_amdgcn_mfma_f32_32x32x16_bf16(kf[d0], qf[8 + d0], p0, 0, 0, 0);
; #pragma unroll
;     for (int r = 0; r < 16; ++r) sc[r] = fmaf(w[1], relu_i(p1[r]), sc[r]);
;     p1 = f32x16{};
; #pragma unroll
;     for (int d0 = 0; d0 < 4; ++d0) p1 = __builtin_amdgcn_mfma_f32_32x32x16_bf16(kf[d0], qf[12 + d0], p1, 0, 0, 0);
; #pragma unroll
;     for (int r = 0; r < 16; ++r) sc[r] = fmaf(w[2], relu_i(p0[r]), sc[r]);
; #pragma unroll
;     for (int r = 0; r < 16; ++r) sc[r] = fmaf(w[3], relu_i(p1[r]), sc[r]);
; }
; template <int PASS> __device__ __forceinline__ void idx_pass(const bf16_t* KIb, const bf16x8 (&qf)[16], const f32x4& w, int jd, int tq, int wid, int r32, int hi, unsigned khi, unsigned klo, bool cand, LAS unsigned char* L) {
;     ...
;         idx_scores_k(sc, kB, qf, w);
;         if (diag) idx_half<PASS, true>(hw, ehw, sc, j * 64 + 32, tq, r32, hi, khi, klo, cand, L); else idx_half<PASS, false>(hw, ehw, sc, j * 64 + 32, tq, r32, hi, khi, klo, cand, L);
.LBB0_1131:
	s_mov_b64 s[14:15], -1
	s_and_b64 vcc, exec, s[18:19]
	s_waitcnt vmcnt(3)
	v_mfma_f32_32x32x16_bf16 v[2:17], v[46:49], v[70:73], 0
	s_waitcnt vmcnt(2)
	v_mfma_f32_32x32x16_bf16 v[2:17], v[42:45], v[74:77], v[2:17]
	s_waitcnt vmcnt(1)
	v_mfma_f32_32x32x16_bf16 v[2:17], v[38:41], v[78:81], v[2:17]
	s_waitcnt vmcnt(0)
	v_mfma_f32_32x32x16_bf16 v[2:17], v[34:37], v[82:85], v[2:17]
	v_mfma_f32_32x32x16_bf16 v[180:195], v[46:49], v[86:89], 0
	v_mfma_f32_32x32x16_bf16 v[180:195], v[42:45], v[90:93], v[180:195]
	v_mfma_f32_32x32x16_bf16 v[180:195], v[38:41], v[94:97], v[180:195]
	v_mfma_f32_32x32x16_bf16 v[180:195], v[34:37], v[98:101], v[180:195]
	s_nop 7
	v_max_i32_e32 v196, 0, v2
	v_mul_f32_e32 v53, v66, v196
	v_max_i32_e32 v196, 0, v3
	v_mul_f32_e32 v54, v66, v196
	v_max_i32_e32 v196, 0, v4
	v_mul_f32_e32 v55, v66, v196
	v_max_i32_e32 v196, 0, v5
	v_mul_f32_e32 v56, v66, v196
	v_max_i32_e32 v196, 0, v6
	v_mul_f32_e32 v57, v66, v196
	v_max_i32_e32 v196, 0, v7
	v_mul_f32_e32 v58, v66, v196
	v_max_i32_e32 v196, 0, v8
	v_mul_f32_e32 v59, v66, v196
	v_max_i32_e32 v196, 0, v9
	v_mul_f32_e32 v60, v66, v196
	v_max_i32_e32 v196, 0, v10
	v_mul_f32_e32 v61, v66, v196
	v_max_i32_e32 v196, 0, v11
	v_mul_f32_e32 v62, v66, v196
	v_max_i32_e32 v196, 0, v12
	v_mul_f32_e32 v63, v66, v196
	v_max_i32_e32 v196, 0, v13
	v_mul_f32_e32 v64, v66, v196
	v_max_i32_e32 v196, 0, v14
	v_mul_f32_e32 v65, v66, v196
	v_max_i32_e32 v196, 0, v15
	v_mul_f32_e32 v144, v66, v196
	v_max_i32_e32 v196, 0, v16
	v_mul_f32_e32 v145, v66, v196
	v_max_i32_e32 v196, 0, v17
	v_mul_f32_e32 v146, v66, v196
	v_mfma_f32_32x32x16_bf16 v[2:17], v[46:49], v[102:105], 0
	v_mfma_f32_32x32x16_bf16 v[2:17], v[42:45], v[106:109], v[2:17]
	v_mfma_f32_32x32x16_bf16 v[2:17], v[38:41], v[110:113], v[2:17]
	v_mfma_f32_32x32x16_bf16 v[2:17], v[34:37], v[114:117], v[2:17]
	v_max_i32_e32 v196, 0, v180
	v_fmac_f32_e32 v53, v67, v196
	v_max_i32_e32 v196, 0, v181
	v_fmac_f32_e32 v54, v67, v196
	v_max_i32_e32 v196, 0, v182
	v_fmac_f32_e32 v55, v67, v196
	v_max_i32_e32 v196, 0, v183
	v_fmac_f32_e32 v56, v67, v196
	v_max_i32_e32 v196, 0, v184
	v_fmac_f32_e32 v57, v67, v196
	v_max_i32_e32 v196, 0, v185
	v_fmac_f32_e32 v58, v67, v196
	v_max_i32_e32 v196, 0, v186
	v_fmac_f32_e32 v59, v67, v196
	v_max_i32_e32 v196, 0, v187
	v_fmac_f32_e32 v60, v67, v196
	v_max_i32_e32 v196, 0, v188
	v_fmac_f32_e32 v61, v67, v196
	v_max_i32_e32 v196, 0, v189
	v_fmac_f32_e32 v62, v67, v196
	v_max_i32_e32 v196, 0, v190
	v_fmac_f32_e32 v63, v67, v196
	v_max_i32_e32 v196, 0, v191
	v_fmac_f32_e32 v64, v67, v196
	v_max_i32_e32 v196, 0, v192
	v_fmac_f32_e32 v65, v67, v196
	v_max_i32_e32 v196, 0, v193
	v_fmac_f32_e32 v144, v67, v196
	v_max_i32_e32 v196, 0, v194
	v_fmac_f32_e32 v145, v67, v196
	v_max_i32_e32 v196, 0, v195
	v_fmac_f32_e32 v146, v67, v196
	v_mfma_f32_32x32x16_bf16 v[180:195], v[46:49], v[118:121], 0
	v_mfma_f32_32x32x16_bf16 v[180:195], v[42:45], v[122:125], v[180:195]
	v_mfma_f32_32x32x16_bf16 v[180:195], v[38:41], v[126:129], v[180:195]
	v_mfma_f32_32x32x16_bf16 v[180:195], v[34:37], v[130:133], v[180:195]
	v_max_i32_e32 v196, 0, v2
	v_fmac_f32_e32 v53, v68, v196
	v_max_i32_e32 v196, 0, v3
	v_fmac_f32_e32 v54, v68, v196
	v_max_i32_e32 v196, 0, v4
	v_fmac_f32_e32 v55, v68, v196
	v_max_i32_e32 v196, 0, v5
	v_fmac_f32_e32 v56, v68, v196
	v_max_i32_e32 v196, 0, v6
	v_fmac_f32_e32 v57, v68, v196
	v_max_i32_e32 v196, 0, v7
	v_fmac_f32_e32 v58, v68, v196
	v_max_i32_e32 v196, 0, v8
	v_fmac_f32_e32 v59, v68, v196
	v_max_i32_e32 v196, 0, v9
	v_fmac_f32_e32 v60, v68, v196
	v_max_i32_e32 v196, 0, v10
	v_fmac_f32_e32 v61, v68, v196
	v_max_i32_e32 v196, 0, v11
	v_fmac_f32_e32 v62, v68, v196
	v_max_i32_e32 v196, 0, v12
	v_fmac_f32_e32 v63, v68, v196
	v_max_i32_e32 v196, 0, v13
	v_fmac_f32_e32 v64, v68, v196
	v_max_i32_e32 v196, 0, v14
	v_fmac_f32_e32 v65, v68, v196
	v_max_i32_e32 v196, 0, v15
	v_fmac_f32_e32 v144, v68, v196
	v_max_i32_e32 v196, 0, v16
	v_fmac_f32_e32 v145, v68, v196
	v_max_i32_e32 v196, 0, v17
	v_fmac_f32_e32 v146, v68, v196
	v_max_i32_e32 v196, 0, v180
	v_fmac_f32_e32 v53, v69, v196
	v_max_i32_e32 v196, 0, v181
	v_fmac_f32_e32 v54, v69, v196
	v_max_i32_e32 v196, 0, v182
	v_fmac_f32_e32 v55, v69, v196
	v_max_i32_e32 v196, 0, v183
	v_fmac_f32_e32 v56, v69, v196
	v_max_i32_e32 v196, 0, v184
	v_fmac_f32_e32 v57, v69, v196
	v_max_i32_e32 v196, 0, v185
	v_fmac_f32_e32 v58, v69, v196
	v_max_i32_e32 v196, 0, v186
	v_fmac_f32_e32 v59, v69, v196
	v_max_i32_e32 v196, 0, v187
	v_fmac_f32_e32 v60, v69, v196
	v_max_i32_e32 v196, 0, v188
	v_fmac_f32_e32 v61, v69, v196
	v_max_i32_e32 v196, 0, v189
	v_fmac_f32_e32 v62, v69, v196
	v_max_i32_e32 v196, 0, v190
	v_fmac_f32_e32 v63, v69, v196
	v_max_i32_e32 v196, 0, v191
	v_fmac_f32_e32 v64, v69, v196
	v_max_i32_e32 v196, 0, v192
	v_fmac_f32_e32 v65, v69, v196
	v_max_i32_e32 v196, 0, v193
	v_fmac_f32_e32 v144, v69, v196
	v_max_i32_e32 v196, 0, v194
	v_fmac_f32_e32 v145, v69, v196
	v_max_i32_e32 v196, 0, v195
	v_fmac_f32_e32 v146, v69, v196
	s_cbranch_vccz .LBB0_1196
; #define LAS __attribute__((address_space(3)))
; __device__ __forceinline__ int crow(int r, int hi) { return (r & 3) + 8 * (r >> 2) + 4 * hi; }
; __device__ __forceinline__ unsigned fkey2(float v) { const unsigned u = __float_as_uint(v + 0.0f); return u ^ ((unsigned)((int)u >> 31) | 0x80000000u); }
; __device__ __forceinline__ void shl_ge(unsigned& acc, unsigned key, unsigned thr) { asm("v_cmp_ge_u32 vcc, %1, %2\n\tv_addc_co_u32 %0, vcc, %0, %0, vcc" : "+v"(acc) : "v"(key), "v"(thr) : "vcc"); }
; __device__ __forceinline__ unsigned spread4(unsigned x) { return (x & 0xFu) | ((x & 0xF0u) << 4) | ((x & 0xF00u) << 8) | ((x & 0xF000u) << 12); }
; template <int PASS, bool DIAG> __device__ __forceinline__ void idx_half(unsigned& bits, unsigned& ebits, const f32x16& sc, int sbase, int tq, int r32, int hi, unsigned khi, unsigned klo, bool cand, LAS unsigned char* L) {
;     ...
;         unsigned hb = 0u, lb = 0u;
; #pragma unroll
;         for (int r = 15; r >= 0; --r) { const unsigned key = fkey2(sc[r]); shl_ge(hb, key, khi); shl_ge(lb, key, klo); }
;         bits = spread4(hb); ebits = spread4(lb & ~hb);
;         if (DIAG) { const unsigned vm = d < 0 ? 0u : (d >= 31 ? 0xFFFFFFFFu : ((2u << d) - 1u)); bits &= vm; ebits &= vm; }
;         if (cand && ebits != 0u) {
;             unsigned slot = __hip_atomic_fetch_add((LAS unsigned*)(L + IL_CNT) + r32, (unsigned)__builtin_popcount(ebits), __ATOMIC_RELAXED, __HIP_MEMORY_SCOPE_WORKGROUP);
; #pragma unroll
;             for (int r = 0; r < 16; ++r) if ((ebits >> crow(r, 0)) & 1u) { const int s = sbase + crow(r, hi);
;                 if (slot < (unsigned)IDX_CAP) ((LAS unsigned long long*)(L + IL_CAND))[r32 * IDX_CAP + slot] = ((unsigned long long)fkey2(sc[r]) << 16) | (unsigned long long)(0xFFFFu - (unsigned)s);
;                 ++slot; }
	v_add_f32_e32 v0, 0, v146
	v_ashrrev_i32_e32 v2, 31, v0
	v_bitop3_b32 v2, v2, v0, s85 bitop3:0x36
	v_add_f32_e32 v0, 0, v145
	v_ashrrev_i32_e32 v3, 31, v0
	v_bitop3_b32 v4, v3, v0, s85 bitop3:0x36
	v_add_f32_e32 v0, 0, v144
	v_ashrrev_i32_e32 v3, 31, v0
	v_bitop3_b32 v6, v3, v0, s85 bitop3:0x36
	v_add_f32_e32 v0, 0, v65
	v_ashrrev_i32_e32 v3, 31, v0
	v_bitop3_b32 v8, v3, v0, s85 bitop3:0x36
	v_add_f32_e32 v0, 0, v64
	v_ashrrev_i32_e32 v3, 31, v0
	v_bitop3_b32 v10, v3, v0, s85 bitop3:0x36
	v_add_f32_e32 v0, 0, v63
	v_ashrrev_i32_e32 v3, 31, v0
	v_bitop3_b32 v12, v3, v0, s85 bitop3:0x36
	v_add_f32_e32 v0, 0, v62
	v_ashrrev_i32_e32 v3, 31, v0
	v_bitop3_b32 v14, v3, v0, s85 bitop3:0x36
	v_add_f32_e32 v0, 0, v61
	v_ashrrev_i32_e32 v3, 31, v0
	v_mov_b32_e32 v49, 0
	v_mov_b32_e32 v5, 0
	v_bitop3_b32 v16, v3, v0, s85 bitop3:0x36
	v_add_f32_e32 v0, 0, v60
	v_cmp_ge_u32 vcc, v2, v135
	v_addc_co_u32 v49, vcc, v49, v49, vcc
	v_ashrrev_i32_e32 v3, 31, v0
	v_cmp_ge_u32 vcc, v2, v134
	v_addc_co_u32 v5, vcc, v5, v5, vcc
	v_bitop3_b32 v34, v3, v0, s85 bitop3:0x36
	v_cmp_ge_u32 vcc, v4, v135
	v_addc_co_u32 v49, vcc, v49, v49, vcc
	v_add_f32_e32 v0, 0, v59
	v_cmp_ge_u32 vcc, v4, v134
	v_addc_co_u32 v5, vcc, v5, v5, vcc
	v_ashrrev_i32_e32 v3, 31, v0
	v_cmp_ge_u32 vcc, v6, v135
	v_addc_co_u32 v49, vcc, v49, v49, vcc
	v_bitop3_b32 v36, v3, v0, s85 bitop3:0x36
	v_cmp_ge_u32 vcc, v6, v134
	v_addc_co_u32 v5, vcc, v5, v5, vcc
	v_add_f32_e32 v0, 0, v58
	v_cmp_ge_u32 vcc, v8, v135
	v_addc_co_u32 v49, vcc, v49, v49, vcc
	v_ashrrev_i32_e32 v3, 31, v0
	v_cmp_ge_u32 vcc, v8, v134
	v_addc_co_u32 v5, vcc, v5, v5, vcc
	v_bitop3_b32 v38, v3, v0, s85 bitop3:0x36
	v_cmp_ge_u32 vcc, v10, v135
	v_addc_co_u32 v49, vcc, v49, v49, vcc
	v_add_f32_e32 v0, 0, v57
	v_cmp_ge_u32 vcc, v10, v134
	v_addc_co_u32 v5, vcc, v5, v5, vcc
	v_ashrrev_i32_e32 v3, 31, v0
	v_cmp_ge_u32 vcc, v12, v135
	v_addc_co_u32 v49, vcc, v49, v49, vcc
	v_bitop3_b32 v40, v3, v0, s85 bitop3:0x36
	v_cmp_ge_u32 vcc, v12, v134
	v_addc_co_u32 v5, vcc, v5, v5, vcc
	v_add_f32_e32 v0, 0, v56
	v_cmp_ge_u32 vcc, v14, v135
	v_addc_co_u32 v49, vcc, v49, v49, vcc
	v_ashrrev_i32_e32 v3, 31, v0
	v_cmp_ge_u32 vcc, v14, v134
	v_addc_co_u32 v5, vcc, v5, v5, vcc
	v_bitop3_b32 v42, v3, v0, s85 bitop3:0x36
	v_cmp_ge_u32 vcc, v16, v135
	v_addc_co_u32 v49, vcc, v49, v49, vcc
	v_add_f32_e32 v0, 0, v55
	v_cmp_ge_u32 vcc, v16, v134
	v_addc_co_u32 v5, vcc, v5, v5, vcc
	v_ashrrev_i32_e32 v3, 31, v0
	v_cmp_ge_u32 vcc, v34, v135
	v_addc_co_u32 v49, vcc, v49, v49, vcc
	v_bitop3_b32 v44, v3, v0, s85 bitop3:0x36
	v_cmp_ge_u32 vcc, v34, v134
	v_addc_co_u32 v5, vcc, v5, v5, vcc
	v_add_f32_e32 v0, 0, v54
	v_cmp_ge_u32 vcc, v36, v135
	v_addc_co_u32 v49, vcc, v49, v49, vcc
	v_ashrrev_i32_e32 v3, 31, v0
	v_cmp_ge_u32 vcc, v36, v134
	v_addc_co_u32 v5, vcc, v5, v5, vcc
	v_bitop3_b32 v46, v3, v0, s85 bitop3:0x36
	v_cmp_ge_u32 vcc, v38, v135
	v_addc_co_u32 v49, vcc, v49, v49, vcc
	v_add_f32_e32 v0, 0, v53
	v_cmp_ge_u32 vcc, v38, v134
	v_addc_co_u32 v5, vcc, v5, v5, vcc
	v_ashrrev_i32_e32 v3, 31, v0
	v_cmp_ge_u32 vcc, v40, v135
	v_addc_co_u32 v49, vcc, v49, v49, vcc
	v_bitop3_b32 v0, v3, v0, s85 bitop3:0x36
	v_cmp_ge_u32 vcc, v40, v134
	v_addc_co_u32 v5, vcc, v5, v5, vcc
	s_nop 0
	v_cmp_ge_u32 vcc, v42, v135
	v_addc_co_u32 v49, vcc, v49, v49, vcc
	s_nop 0
	v_cmp_ge_u32 vcc, v42, v134
	v_addc_co_u32 v5, vcc, v5, v5, vcc
	s_nop 0
	v_cmp_ge_u32 vcc, v44, v135
	v_addc_co_u32 v49, vcc, v49, v49, vcc
	s_nop 0
	v_cmp_ge_u32 vcc, v44, v134
	v_addc_co_u32 v5, vcc, v5, v5, vcc
	s_nop 0
	v_cmp_ge_u32 vcc, v46, v135
	v_addc_co_u32 v49, vcc, v49, v49, vcc
	s_nop 0
	v_cmp_ge_u32 vcc, v46, v134
	v_addc_co_u32 v5, vcc, v5, v5, vcc
	s_nop 0
	v_cmp_ge_u32 vcc, v0, v135
	v_addc_co_u32 v49, vcc, v49, v49, vcc
	s_nop 0
	v_cmp_ge_u32 vcc, v0, v134
	v_addc_co_u32 v5, vcc, v5, v5, vcc
	s_nop 0
	v_bitop3_b32 v3, v5, v49, v5 bitop3:0x30
	v_bitop3_b32 v5, v5, 15, v49 bitop3:0x40
	v_lshlrev_b32_e32 v7, 4, v3
	v_and_or_b32 v5, v7, s93, v5
	v_lshlrev_b32_e32 v7, 8, v3
	v_lshlrev_b32_e32 v9, 12, v3
	v_and_b32_e32 v7, 0xf0000, v7
	v_and_b32_e32 v9, 0xf000000, v9
	v_or3_b32 v48, v5, v7, v9
	v_cmp_ne_u32_e32 vcc, 0, v48
	s_and_b64 s[0:1], s[10:11], vcc
	s_and_saveexec_b64 s[18:19], s[0:1]
	s_cbranch_execz .LBB0_1195
	v_bcnt_u32_b32 v5, v48, 0
	ds_add_rtn_u32 v147, v221, v5
	v_and_b32_e32 v5, 1, v3
	v_cmp_eq_u32_e32 vcc, 1, v5
	s_and_saveexec_b64 s[14:15], vcc
	s_cbranch_execz .LBB0_1137
	s_waitcnt lgkmcnt(0)
	v_cmp_gt_u32_e32 vcc, s87, v147
	s_and_saveexec_b64 s[42:43], vcc
	s_cbranch_execz .LBB0_1136
	v_lshlrev_b64 v[148:149], 16, v[0:1]
	v_add_u32_e32 v0, s45, v142
	v_subrev_u32_e32 v0, 32, v0
	v_lshl_add_u32 v5, v147, 3, v136
	v_or_b32_e32 v148, v148, v0
	ds_write_b64 v5, v[148:149] offset:512
